# speedup vs baseline: 1.0159x; 1.0026x over previous
.LBB2_22:
	ds_read_b128 v[170:173], v174
	ds_read_b128 v[180:183], v174 offset:2048
	ds_read_b128 v[202:205], v178
	ds_read_b128 v[206:209], v178 offset:2048
	s_mov_b32 s89, s65
	s_mov_b32 s65, s6
	ds_read_b128 v[162:165], v194
	ds_read_b128 v[150:153], v194 offset:2048
	ds_read_b128 v[166:169], v195
	ds_read_b128 v[154:157], v195 offset:2048
	ds_read_b128 v[146:149], v194 offset:4096
	ds_read_b128 v[138:141], v194 offset:6144
	ds_read_b128 v[158:161], v195 offset:4096
	ds_read_b128 v[142:145], v195 offset:6144
	s_waitcnt vmcnt(14)
	s_mul_i32 s94, s83, s35
	v_cvt_pk_f16_f32 v22, v22, v23
	v_cvt_pk_f16_f32 v23, v24, v25
	v_cvt_pk_f16_f32 v18, v18, v19
	v_cvt_pk_f16_f32 v19, v20, v21
	v_cvt_pk_f16_f32 v14, v14, v15
	v_cvt_pk_f16_f32 v15, v16, v17
	v_cvt_pk_f16_f32 v10, v10, v11
	v_cvt_pk_f16_f32 v11, v12, v13
	ds_write2st64_b64 v201, v[22:23], v[18:19] offset0:32 offset1:40
	ds_write2st64_b64 v201, v[14:15], v[10:11] offset0:48 offset1:56
	s_nop 0
	s_lshl_b32 s6, s90, 6
	s_add_i32 s7, s94, s6
	s_lshl_b32 s7, s7, 2
	s_add_i32 s8, s7, s81
	buffer_load_dwordx4 v[22:25], v192, s[56:59], s7 offen nt
	buffer_load_dwordx4 v[18:21], v192, s[56:59], s8 offen nt
	s_waitcnt vmcnt(14)
	v_add_u32_e32 v210, s89, v193
	s_mul_i32 s95, s84, s35
	ds_write_b128 v210, v[6:9] offset:32768
	ds_write_b128 v210, v[2:5] offset:40960
	s_add_i32 s9, s8, s81
	s_add_i32 s93, s95, s6
	s_add_i32 s10, s9, s81
	buffer_load_dwordx4 v[14:17], v192, s[56:59], s9 offen nt
	buffer_load_dwordx4 v[10:13], v192, s[56:59], s10 offen nt
	s_barrier
	s_waitcnt lgkmcnt(0)
	s_setprio 1
	s_waitcnt lgkmcnt(11)
	v_mfma_f32_16x16x32_f16 v[134:137], v[170:173], v[162:165], v[134:137]
	v_mfma_f32_16x16x32_f16 v[130:133], v[180:183], v[162:165], v[130:133]
	s_waitcnt lgkmcnt(10)
	v_mfma_f32_16x16x32_f16 v[126:129], v[170:173], v[150:153], v[126:129]
	v_mfma_f32_16x16x32_f16 v[122:125], v[180:183], v[150:153], v[122:125]
	s_waitcnt lgkmcnt(7)
	v_mfma_f32_16x16x32_f16 v[118:121], v[170:173], v[146:149], v[118:121]
	v_mfma_f32_16x16x32_f16 v[114:117], v[180:183], v[146:149], v[114:117]
	s_waitcnt lgkmcnt(6)
	v_mfma_f32_16x16x32_f16 v[110:113], v[170:173], v[138:141], v[110:113]
	v_mfma_f32_16x16x32_f16 v[106:109], v[180:183], v[138:141], v[106:109]
	v_mfma_f32_16x16x32_f16 v[134:137], v[202:205], v[166:169], v[134:137]
	v_mfma_f32_16x16x32_f16 v[130:133], v[206:209], v[166:169], v[130:133]
	v_mfma_f32_16x16x32_f16 v[126:129], v[202:205], v[154:157], v[126:129]
	v_mfma_f32_16x16x32_f16 v[122:125], v[206:209], v[154:157], v[122:125]
	s_waitcnt lgkmcnt(5)
	v_mfma_f32_16x16x32_f16 v[118:121], v[202:205], v[158:161], v[118:121]
	v_mfma_f32_16x16x32_f16 v[114:117], v[206:209], v[158:161], v[114:117]
	s_waitcnt lgkmcnt(4)
	v_mfma_f32_16x16x32_f16 v[110:113], v[202:205], v[142:145], v[110:113]
	v_mfma_f32_16x16x32_f16 v[106:109], v[206:209], v[142:145], v[106:109]
	s_setprio 0
	s_barrier
	ds_read_b128 v[170:173], v174 offset:16384
	ds_read_b128 v[174:177], v174 offset:18432
	ds_read_b128 v[182:185], v178 offset:16384
	ds_read_b128 v[178:181], v178 offset:18432
	s_waitcnt vmcnt(14)
	s_cmp_lt_u32 s92, 32
	ds_write_b128 v210, v[30:33] offset:49152
	ds_write_b128 v210, v[26:29] offset:57344
	s_waitcnt vmcnt(13)
	s_cbranch_scc0 .LBB2_28
	s_add_i32 s38, s64, s92
	s_lshl_b64 s[60:61], s[38:39], 3
	s_add_u32 s60, s60, s85
	v_cmp_ne_u32_e64 s[6:7], 0, v34
	v_cmp_ne_u32_e64 s[8:9], 0, v35
	v_cmp_ne_u32_e64 s[10:11], 0, v36
	v_cmp_ne_u32_e64 s[12:13], 0, v37
	s_addc_u32 s61, s61, 0
	s_nop 1
	s_and_b64 s[98:99], s[6:7], s[8:9]
	s_and_b64 s[100:101], s[10:11], s[12:13]
	s_and_b64 s[98:99], s[98:99], s[100:101]
	s_cmp_eq_u64 s[98:99], -1
	s_cbranch_scc0 .Lqkv_mslow_0
	s_lshl_b64 s[96:97], s[60:61], 5
	v_lshl_add_u64 v[26:27], v[0:1], 0, s[96:97]
	v_mov_b32_e32 v28, -1
	v_mov_b32_e32 v29, -1
	s_add_u32 s6, s42, s60
	s_addc_u32 s7, s43, s61
	s_mov_b64 exec, 15
	global_store_dwordx2 v[26:27], v[28:29], off
	s_mov_b64 exec, 1
	global_store_byte v187, v187, s[6:7]
	s_mov_b64 exec, -1
	s_branch .LBB2_28

.LBB2_33:
	s_barrier
	s_waitcnt lgkmcnt(0)
	s_setprio 1
	s_waitcnt lgkmcnt(5)
	v_mfma_f32_16x16x32_f16 v[102:105], v[170:173], v[162:165], v[102:105]
	s_waitcnt lgkmcnt(4)
	v_mfma_f32_16x16x32_f16 v[98:101], v[174:177], v[162:165], v[98:101]
	v_mfma_f32_16x16x32_f16 v[94:97], v[170:173], v[150:153], v[94:97]
	v_mfma_f32_16x16x32_f16 v[90:93], v[174:177], v[150:153], v[90:93]
	v_mfma_f32_16x16x32_f16 v[86:89], v[170:173], v[146:149], v[86:89]
	v_mfma_f32_16x16x32_f16 v[82:85], v[174:177], v[146:149], v[82:85]
	v_mfma_f32_16x16x32_f16 v[78:81], v[170:173], v[138:141], v[78:81]
	v_mfma_f32_16x16x32_f16 v[74:77], v[174:177], v[138:141], v[74:77]
	s_waitcnt lgkmcnt(3)
	v_mfma_f32_16x16x32_f16 v[102:105], v[182:185], v[166:169], v[102:105]
	s_waitcnt lgkmcnt(2)
	v_mfma_f32_16x16x32_f16 v[98:101], v[178:181], v[166:169], v[98:101]
	v_mfma_f32_16x16x32_f16 v[94:97], v[182:185], v[154:157], v[94:97]
	v_mfma_f32_16x16x32_f16 v[90:93], v[178:181], v[154:157], v[90:93]
	v_mfma_f32_16x16x32_f16 v[86:89], v[182:185], v[158:161], v[86:89]
	v_mfma_f32_16x16x32_f16 v[82:85], v[178:181], v[158:161], v[82:85]
	v_mfma_f32_16x16x32_f16 v[78:81], v[182:185], v[142:145], v[78:81]
	v_mfma_f32_16x16x32_f16 v[74:77], v[178:181], v[142:145], v[74:77]
	s_setprio 0
	s_barrier
	v_add_u32_e32 v202, s89, v196
	v_add_u32_e32 v203, s89, v186
	ds_read_b128 v[170:173], v202 offset:32768
	ds_read_b128 v[174:177], v202 offset:34816
	ds_read_b128 v[178:181], v203 offset:32768
	ds_read_b128 v[182:185], v203 offset:34816
	ds_read_b128 v[162:165], v194 offset:16384
	ds_read_b128 v[150:153], v194 offset:18432
	ds_read_b128 v[166:169], v195 offset:16384
	ds_read_b128 v[154:157], v195 offset:18432
	ds_read_b128 v[146:149], v194 offset:20480
	ds_read_b128 v[138:141], v194 offset:22528
	ds_read_b128 v[158:161], v195 offset:20480
	ds_read_b128 v[142:145], v195 offset:22528
	s_waitcnt vmcnt(14)
	s_lshl_b32 s86, s90, 6
	v_cvt_pk_f16_f32 v58, v58, v59
	v_cvt_pk_f16_f32 v59, v60, v61
	v_cvt_pk_f16_f32 v54, v54, v55
	v_cvt_pk_f16_f32 v55, v56, v57
	v_cvt_pk_f16_f32 v50, v50, v51
	v_cvt_pk_f16_f32 v51, v52, v53
	v_cvt_pk_f16_f32 v46, v46, v47
	v_cvt_pk_f16_f32 v47, v48, v49
	ds_write2st64_b64 v201, v[58:59], v[54:55] offset1:8
	ds_write2st64_b64 v201, v[50:51], v[46:47] offset0:16 offset1:24
	s_nop 0
	s_add_i32 s6, s94, s86
	s_lshl_b32 s6, s6, 2
	s_add_i32 s7, s6, s81
	buffer_load_dwordx4 v[58:61], v192, s[56:59], s6 offen nt
	buffer_load_dwordx4 v[54:57], v192, s[56:59], s7 offen nt
	s_waitcnt vmcnt(14)
	v_add_u32_e32 v204, s87, v193
	ds_write_b128 v204, v[42:45] offset:32768
	ds_write_b128 v204, v[38:41] offset:40960
	s_add_i32 s8, s7, s81
	s_add_i32 s9, s8, s81
	buffer_load_dwordx4 v[50:53], v192, s[56:59], s8 offen nt
	buffer_load_dwordx4 v[46:49], v192, s[56:59], s9 offen nt
	s_barrier
	s_waitcnt lgkmcnt(0)
	s_setprio 1
	s_waitcnt lgkmcnt(11)
	v_mfma_f32_16x16x32_f16 v[134:137], v[170:173], v[162:165], v[134:137]
	v_mfma_f32_16x16x32_f16 v[130:133], v[174:177], v[162:165], v[130:133]
	s_waitcnt lgkmcnt(10)
	v_mfma_f32_16x16x32_f16 v[126:129], v[170:173], v[150:153], v[126:129]
	v_mfma_f32_16x16x32_f16 v[122:125], v[174:177], v[150:153], v[122:125]
	s_waitcnt lgkmcnt(7)
	v_mfma_f32_16x16x32_f16 v[118:121], v[170:173], v[146:149], v[118:121]
	v_mfma_f32_16x16x32_f16 v[114:117], v[174:177], v[146:149], v[114:117]
	s_waitcnt lgkmcnt(6)
	v_mfma_f32_16x16x32_f16 v[110:113], v[170:173], v[138:141], v[110:113]
	v_mfma_f32_16x16x32_f16 v[106:109], v[174:177], v[138:141], v[106:109]
	v_mfma_f32_16x16x32_f16 v[134:137], v[178:181], v[166:169], v[134:137]
	v_mfma_f32_16x16x32_f16 v[130:133], v[182:185], v[166:169], v[130:133]
	v_mfma_f32_16x16x32_f16 v[126:129], v[178:181], v[154:157], v[126:129]
	v_mfma_f32_16x16x32_f16 v[122:125], v[182:185], v[154:157], v[122:125]
	s_waitcnt lgkmcnt(5)
	v_mfma_f32_16x16x32_f16 v[118:121], v[178:181], v[158:161], v[118:121]
	v_mfma_f32_16x16x32_f16 v[114:117], v[182:185], v[158:161], v[114:117]
	s_waitcnt lgkmcnt(4)
	v_mfma_f32_16x16x32_f16 v[110:113], v[178:181], v[142:145], v[110:113]
	v_mfma_f32_16x16x32_f16 v[106:109], v[182:185], v[142:145], v[106:109]
	s_setprio 0
	s_barrier
	ds_read_b128 v[170:173], v202 offset:49152
	ds_read_b128 v[174:177], v202 offset:51200
	ds_read_b128 v[182:185], v203 offset:49152
	ds_read_b128 v[178:181], v203 offset:51200
	s_waitcnt vmcnt(14)
	s_cmp_gt_u32 s92, 30
	ds_write_b128 v204, v[66:69] offset:49152
	ds_write_b128 v204, v[62:65] offset:57344
	s_waitcnt vmcnt(13)
	s_cbranch_scc1 .LBB2_39
	s_add_i32 s38, s64, s92
	s_add_i32 s38, s38, 1
	s_lshl_b64 s[60:61], s[38:39], 3
	s_add_u32 s60, s60, s85
	v_cmp_ne_u32_e64 s[6:7], 0, v70
	v_cmp_ne_u32_e64 s[8:9], 0, v71
	v_cmp_ne_u32_e64 s[10:11], 0, v72
	v_cmp_ne_u32_e64 s[12:13], 0, v73
	s_addc_u32 s61, s61, 0
	s_nop 1
	s_and_b64 s[98:99], s[6:7], s[8:9]
	s_and_b64 s[100:101], s[10:11], s[12:13]
	s_and_b64 s[98:99], s[98:99], s[100:101]
	s_cmp_eq_u64 s[98:99], -1
	s_cbranch_scc0 .Lqkv_mslow_1
	s_lshl_b64 s[94:95], s[60:61], 5
	v_lshl_add_u64 v[62:63], v[0:1], 0, s[94:95]
	v_mov_b32_e32 v64, -1
	v_mov_b32_e32 v65, -1
	s_add_u32 s6, s42, s60
	s_addc_u32 s7, s43, s61
	s_mov_b64 exec, 15
	global_store_dwordx2 v[62:63], v[64:65], off
	s_mov_b64 exec, 1
	global_store_byte v187, v187, s[6:7]
	s_mov_b64 exec, -1
	s_branch .LBB2_39
